# v10 + own phase-2 block-conversion loop (two jobs of loads in flight, plain write-back stores)
# speedup vs baseline: 1.0222x; 1.0003x over previous
; #define LAS __attribute__((address_space(3)))
; #define BJOB_LD(p) __builtin_nontemporal_load(p)
; __device__ __forceinline__ BJob bjob_addr(const Args& a, int j) {
;     BJob c;
;     if (j < CONV_JOBS_GU) { const int e = j >> 8, kb = (j >> 4) & 15, nb = j & 15; c.s0 = nb * 256; c.gu = 1;
;         c.src = a.w_gate_up + ((size_t)e * 2048 + kb * 128) * 4096 + c.s0; c.ld = 4096; c.dst = (unsigned char*)(a.ws + WS_WGU_T) + (size_t)e * 4096 * 2048 + kb * 128; }
;     else { const int jj = j - CONV_JOBS_GU, e = jj >> 7, kb = (jj >> 3) & 15, nb = jj & 7; c.s0 = nb * 256; c.gu = 0;
;         c.src = a.w_down + ((size_t)e * 2048 + kb * 128) * 2048 + c.s0; c.ld = 2048; c.dst = (unsigned char*)(a.ws + WS_WD_T) + (size_t)e * 2048 * 2048 + kb * 128; }
;     return c;
; }
; __device__ __forceinline__ void bjob_load(const BJob& c, f32x4 (&v)[16]) {
;     int tz = threadIdx.x; asm volatile("" : "+v"(tz));
;     const int w = tz >> 6, lane = tz & 63;
; #pragma unroll
;     for (int r = 0; r < 16; ++r) v[r] = BJOB_LD((const f32x4*)(c.src + (size_t)(w * 16 + r) * c.ld + lane * 4));
; }
; __device__ __forceinline__ void conv_share_blk(const Args& a, LAS unsigned char* lds, int blk, int G) {
;     const int s = blk % 3, r = blk / 3, nb = (G - s + 2) / 3, nj = CONV_JOBS - BJOB0, j0 = BJOB0 + s * (nj / 3), j1 = (s == 2) ? CONV_JOBS : BJOB0 + (s + 1) * (nj / 3);
;     LAS unsigned char* Tlo = lds + 3 * 16384; LAS unsigned char* Thi = lds + LDS_EXTRA;
;     int j = j0 + r; if (j >= j1) return;
;     f32x4 v[16]; u32x4 o[4]; BJob cc = bjob_addr(a, j);
;     bjob_load(cc, v);
; #pragma unroll 1
;     for (;;) {
;         bjob_pack(v, o);
;         const BJob cur = cc; const bool hn = (j + nb) < j1;
;         if (hn) { cc = bjob_addr(a, j + nb); bjob_load(cc, v); }
.Lbc_entry:
	s_waitcnt vmcnt(0)
	v_readfirstlane_b32 s3, v0
	s_nop 3
	s_lshr_b32 s3, s3, 6
	s_cmp_lt_u32 s3, 4
	s_cbranch_scc0 .Lbc_nob0
	s_barrier
.Lbc_nob0:
	v_and_b32_e32 v249, 63, v0
	v_lshlrev_b32_e32 v244, 4, v249
	v_and_b32_e32 v250, 31, v249
	v_lshlrev_b32_e32 v250, 9, v250
	v_and_b32_e32 v251, 7, v249
	v_xor_b32_e32 v251, s3, v251
	v_lshl_add_u32 v250, v251, 4, v250
	v_mov_b32_e32 v251, 0xc000
	v_mov_b32_e32 v252, 0x20400
	v_cmp_gt_u32_e32 vcc, 32, v249
	s_nop 1
	v_cndmask_b32_e32 v251, v252, v251, vcc
	v_add_u32_e32 v245, v250, v251
	v_lshrrev_b32_e32 v250, 3, v0
	v_lshlrev_b32_e32 v251, 7, v250
	v_and_b32_e32 v252, 7, v0
	v_bfe_u32 v253, v0, 5, 3
	v_xor_b32_e32 v253, v252, v253
	v_lshl_add_u32 v251, v253, 4, v251
	v_add_u32_e32 v246, 0xc000, v251
	v_add_u32_e32 v247, 0x20400, v251
	v_lshlrev_b32_e32 v248, 11, v250
	v_lshl_add_u32 v248, v252, 4, v248
	v_readlane_b32 s13, v255, 28
	s_nop 3
	s_addk_i32 s13, 0x1080
	s_mov_b32 s4, 0
	s_cmp_ge_i32 s13, s87
	s_cbranch_scc1 .Lbc_done
	s_lshr_b32 s28, s13, 8
	s_bfe_u32 s30, s13, 0x40004
	s_and_b32 s31, s13, 15
	s_lshl_b32 s28, s28, 25
	s_lshl_b32 s30, s30, 21
	s_add_i32 s28, s28, s30
	s_lshl_b32 s31, s31, 10
	s_add_i32 s28, s28, s31
	s_lshl_b32 s30, s3, 18
	s_add_i32 s28, s28, s30
	s_add_u32 s16, s46, s28
	s_addc_u32 s17, s47, 0
	global_load_dwordx4 v[8:11], v244, s[16:17] nt
	s_add_u32 s16, s16, 0x4000
	s_addc_u32 s17, s17, 0
	global_load_dwordx4 v[12:15], v244, s[16:17] nt
	s_add_u32 s16, s16, 0x4000
	s_addc_u32 s17, s17, 0
	global_load_dwordx4 v[16:19], v244, s[16:17] nt
	s_add_u32 s16, s16, 0x4000
	s_addc_u32 s17, s17, 0
	global_load_dwordx4 v[20:23], v244, s[16:17] nt
	s_add_u32 s16, s16, 0x4000
	s_addc_u32 s17, s17, 0
	global_load_dwordx4 v[24:27], v244, s[16:17] nt
	s_add_u32 s16, s16, 0x4000
	s_addc_u32 s17, s17, 0
	global_load_dwordx4 v[28:31], v244, s[16:17] nt
	s_add_u32 s16, s16, 0x4000
	s_addc_u32 s17, s17, 0
	global_load_dwordx4 v[32:35], v244, s[16:17] nt
	s_add_u32 s16, s16, 0x4000
	s_addc_u32 s17, s17, 0
	global_load_dwordx4 v[36:39], v244, s[16:17] nt
	s_add_u32 s16, s16, 0x4000
	s_addc_u32 s17, s17, 0
	global_load_dwordx4 v[40:43], v244, s[16:17] nt
	s_add_u32 s16, s16, 0x4000
	s_addc_u32 s17, s17, 0
	global_load_dwordx4 v[44:47], v244, s[16:17] nt
	s_add_u32 s16, s16, 0x4000
	s_addc_u32 s17, s17, 0
	global_load_dwordx4 v[48:51], v244, s[16:17] nt
	s_add_u32 s16, s16, 0x4000
	s_addc_u32 s17, s17, 0
	global_load_dwordx4 v[52:55], v244, s[16:17] nt
	s_add_u32 s16, s16, 0x4000
	s_addc_u32 s17, s17, 0
	global_load_dwordx4 v[56:59], v244, s[16:17] nt
	s_add_u32 s16, s16, 0x4000
	s_addc_u32 s17, s17, 0
	global_load_dwordx4 v[60:63], v244, s[16:17] nt
	s_add_u32 s16, s16, 0x4000
	s_addc_u32 s17, s17, 0
	global_load_dwordx4 v[64:67], v244, s[16:17] nt
	s_add_u32 s16, s16, 0x4000
	s_addc_u32 s17, s17, 0
	global_load_dwordx4 v[68:71], v244, s[16:17] nt
	s_add_i32 s33, s13, s89
	s_cmp_ge_i32 s33, s87
	s_cbranch_scc1 .Lbc_p1_none
	s_lshr_b32 s28, s33, 8
	s_bfe_u32 s30, s33, 0x40004
	s_and_b32 s31, s33, 15
	s_lshl_b32 s28, s28, 25
	s_lshl_b32 s30, s30, 21
	s_add_i32 s28, s28, s30
	s_lshl_b32 s31, s31, 10
	s_add_i32 s28, s28, s31
	s_lshl_b32 s30, s3, 18
	s_add_i32 s28, s28, s30
	s_add_u32 s16, s46, s28
	s_addc_u32 s17, s47, 0
	global_load_dwordx4 v[148:151], v244, s[16:17] nt
	s_add_u32 s16, s16, 0x4000
	s_addc_u32 s17, s17, 0
	global_load_dwordx4 v[152:155], v244, s[16:17] nt
	s_add_u32 s16, s16, 0x4000
	s_addc_u32 s17, s17, 0
	global_load_dwordx4 v[156:159], v244, s[16:17] nt
	s_add_u32 s16, s16, 0x4000
	s_addc_u32 s17, s17, 0
	global_load_dwordx4 v[160:163], v244, s[16:17] nt
	s_add_u32 s16, s16, 0x4000
	s_addc_u32 s17, s17, 0
	global_load_dwordx4 v[164:167], v244, s[16:17] nt
	s_add_u32 s16, s16, 0x4000
	s_addc_u32 s17, s17, 0
	global_load_dwordx4 v[168:171], v244, s[16:17] nt
	s_add_u32 s16, s16, 0x4000
	s_addc_u32 s17, s17, 0
	global_load_dwordx4 v[172:175], v244, s[16:17] nt
	s_add_u32 s16, s16, 0x4000
	s_addc_u32 s17, s17, 0
	global_load_dwordx4 v[176:179], v244, s[16:17] nt
	s_add_u32 s16, s16, 0x4000
	s_addc_u32 s17, s17, 0
	global_load_dwordx4 v[180:183], v244, s[16:17] nt
	s_add_u32 s16, s16, 0x4000
	s_addc_u32 s17, s17, 0
	global_load_dwordx4 v[184:187], v244, s[16:17] nt
	s_add_u32 s16, s16, 0x4000
	s_addc_u32 s17, s17, 0
	global_load_dwordx4 v[188:191], v244, s[16:17] nt
	s_add_u32 s16, s16, 0x4000
	s_addc_u32 s17, s17, 0
	global_load_dwordx4 v[192:195], v244, s[16:17] nt
	s_add_u32 s16, s16, 0x4000
	s_addc_u32 s17, s17, 0
	global_load_dwordx4 v[196:199], v244, s[16:17] nt
	s_add_u32 s16, s16, 0x4000
	s_addc_u32 s17, s17, 0
	global_load_dwordx4 v[200:203], v244, s[16:17] nt
	s_add_u32 s16, s16, 0x4000
	s_addc_u32 s17, s17, 0
	global_load_dwordx4 v[204:207], v244, s[16:17] nt
	s_add_u32 s16, s16, 0x4000
	s_addc_u32 s17, s17, 0
	global_load_dwordx4 v[208:211], v244, s[16:17] nt
	s_branch .Lbc_p1_ok
.Lbc_p1_none:
	s_mov_b32 s4, 1
.Lbc_p1_ok:
.Lbc_st_a0:
	s_cmp_lg_u32 s4, 0
	s_cbranch_scc1 .Lbc_w0_a0
	s_waitcnt vmcnt(16)
	s_branch .Lbc_wd_a0

; __device__ __forceinline__ unsigned pk4_fp8_scaled(float a, float b, float c, float d) { s16x2 r = {0, 0}; r = __builtin_amdgcn_cvt_scalef32_pk_fp8_f32(r, a, b, pg8::W8_INV, false); r = __builtin_amdgcn_cvt_scalef32_pk_fp8_f32(r, c, d, pg8::W8_INV, true); return __builtin_bit_cast(unsigned, r); }
; __device__ __forceinline__ void bjob_pack(const f32x4 (&v)[16], u32x4 (&o)[4]) {
; #pragma unroll
;     for (int jn = 0; jn < 4; ++jn) {
;         o[jn].x = pk4_fp8_scaled(v[0][jn], v[1][jn], v[2][jn], v[3][jn]); o[jn].y = pk4_fp8_scaled(v[4][jn], v[5][jn], v[6][jn], v[7][jn]);
;         o[jn].z = pk4_fp8_scaled(v[8][jn], v[9][jn], v[10][jn], v[11][jn]); o[jn].w = pk4_fp8_scaled(v[12][jn], v[13][jn], v[14][jn], v[15][jn]); }
; }
; __device__ __forceinline__ void conv_share_blk(const Args& a, LAS unsigned char* lds, int blk, int G) {
;     ...
; #pragma unroll 1
;     for (;;) {
;         bjob_pack(v, o);
;         const BJob cur = cc; const bool hn = (j + nb) < j1;
;         if (hn) { cc = bjob_addr(a, j + nb); bjob_load(cc, v); }
.Lbc_wd_a0:
	v_cvt_scalef32_pk_fp8_f32 v212, v8, v12, s52
	v_cvt_scalef32_pk_fp8_f32 v213, v24, v28, s52
	v_cvt_scalef32_pk_fp8_f32 v214, v40, v44, s52
	v_cvt_scalef32_pk_fp8_f32 v215, v56, v60, s52
	v_cvt_scalef32_pk_fp8_f32 v216, v9, v13, s52
	v_cvt_scalef32_pk_fp8_f32 v217, v25, v29, s52
	v_cvt_scalef32_pk_fp8_f32 v218, v41, v45, s52
	v_cvt_scalef32_pk_fp8_f32 v219, v57, v61, s52
	v_cvt_scalef32_pk_fp8_f32 v220, v10, v14, s52
	v_cvt_scalef32_pk_fp8_f32 v221, v26, v30, s52
	v_cvt_scalef32_pk_fp8_f32 v222, v42, v46, s52
	v_cvt_scalef32_pk_fp8_f32 v223, v58, v62, s52
	v_cvt_scalef32_pk_fp8_f32 v224, v11, v15, s52
	v_cvt_scalef32_pk_fp8_f32 v225, v27, v31, s52
	v_cvt_scalef32_pk_fp8_f32 v226, v43, v47, s52
	v_cvt_scalef32_pk_fp8_f32 v227, v59, v63, s52
	v_cvt_scalef32_pk_fp8_f32 v212, v16, v20, s52 op_sel:[0,0,0,1]
	v_cvt_scalef32_pk_fp8_f32 v213, v32, v36, s52 op_sel:[0,0,0,1]
	v_cvt_scalef32_pk_fp8_f32 v214, v48, v52, s52 op_sel:[0,0,0,1]
	v_cvt_scalef32_pk_fp8_f32 v215, v64, v68, s52 op_sel:[0,0,0,1]
	v_cvt_scalef32_pk_fp8_f32 v216, v17, v21, s52 op_sel:[0,0,0,1]
	v_cvt_scalef32_pk_fp8_f32 v217, v33, v37, s52 op_sel:[0,0,0,1]
	v_cvt_scalef32_pk_fp8_f32 v218, v49, v53, s52 op_sel:[0,0,0,1]
	v_cvt_scalef32_pk_fp8_f32 v219, v65, v69, s52 op_sel:[0,0,0,1]
	v_cvt_scalef32_pk_fp8_f32 v220, v18, v22, s52 op_sel:[0,0,0,1]
	v_cvt_scalef32_pk_fp8_f32 v221, v34, v38, s52 op_sel:[0,0,0,1]
	v_cvt_scalef32_pk_fp8_f32 v222, v50, v54, s52 op_sel:[0,0,0,1]
	v_cvt_scalef32_pk_fp8_f32 v223, v66, v70, s52 op_sel:[0,0,0,1]
	v_cvt_scalef32_pk_fp8_f32 v224, v19, v23, s52 op_sel:[0,0,0,1]
	v_cvt_scalef32_pk_fp8_f32 v225, v35, v39, s52 op_sel:[0,0,0,1]
	v_cvt_scalef32_pk_fp8_f32 v226, v51, v55, s52 op_sel:[0,0,0,1]
	v_cvt_scalef32_pk_fp8_f32 v227, v67, v71, s52 op_sel:[0,0,0,1]
	s_add_i32 s33, s13, s89
	s_add_i32 s33, s33, s89
	s_cmp_ge_i32 s33, s87
	s_cbranch_scc1 .Lbc_ni_a0
	s_lshr_b32 s28, s33, 8
	s_bfe_u32 s30, s33, 0x40004
	s_and_b32 s31, s33, 15
	s_lshl_b32 s28, s28, 25
	s_lshl_b32 s30, s30, 21
	s_add_i32 s28, s28, s30
	s_lshl_b32 s31, s31, 10
	s_add_i32 s28, s28, s31
	s_lshl_b32 s30, s3, 18
	s_add_i32 s28, s28, s30
	s_add_u32 s16, s46, s28
	s_addc_u32 s17, s47, 0
	global_load_dwordx4 v[8:11], v244, s[16:17] nt
	s_add_u32 s16, s16, 0x4000
	s_addc_u32 s17, s17, 0
	global_load_dwordx4 v[12:15], v244, s[16:17] nt
	s_add_u32 s16, s16, 0x4000
	s_addc_u32 s17, s17, 0
	global_load_dwordx4 v[16:19], v244, s[16:17] nt
	s_add_u32 s16, s16, 0x4000
	s_addc_u32 s17, s17, 0
	global_load_dwordx4 v[20:23], v244, s[16:17] nt
	s_add_u32 s16, s16, 0x4000
	s_addc_u32 s17, s17, 0
	global_load_dwordx4 v[24:27], v244, s[16:17] nt
	s_add_u32 s16, s16, 0x4000
	s_addc_u32 s17, s17, 0
	global_load_dwordx4 v[28:31], v244, s[16:17] nt
	s_add_u32 s16, s16, 0x4000
	s_addc_u32 s17, s17, 0
	global_load_dwordx4 v[32:35], v244, s[16:17] nt
	s_add_u32 s16, s16, 0x4000
	s_addc_u32 s17, s17, 0
	global_load_dwordx4 v[36:39], v244, s[16:17] nt
	s_add_u32 s16, s16, 0x4000
	s_addc_u32 s17, s17, 0
	global_load_dwordx4 v[40:43], v244, s[16:17] nt
	s_add_u32 s16, s16, 0x4000
	s_addc_u32 s17, s17, 0
	global_load_dwordx4 v[44:47], v244, s[16:17] nt
	s_add_u32 s16, s16, 0x4000
	s_addc_u32 s17, s17, 0
	global_load_dwordx4 v[48:51], v244, s[16:17] nt
	s_add_u32 s16, s16, 0x4000
	s_addc_u32 s17, s17, 0
	global_load_dwordx4 v[52:55], v244, s[16:17] nt
	s_add_u32 s16, s16, 0x4000
	s_addc_u32 s17, s17, 0
	global_load_dwordx4 v[56:59], v244, s[16:17] nt
	s_add_u32 s16, s16, 0x4000
	s_addc_u32 s17, s17, 0
	global_load_dwordx4 v[60:63], v244, s[16:17] nt
	s_add_u32 s16, s16, 0x4000
	s_addc_u32 s17, s17, 0
	global_load_dwordx4 v[64:67], v244, s[16:17] nt
	s_add_u32 s16, s16, 0x4000
	s_addc_u32 s17, s17, 0
	global_load_dwordx4 v[68:71], v244, s[16:17] nt
	s_branch .Lbc_io_a0

; #define LAS __attribute__((address_space(3)))
; __device__ __forceinline__ void bjob_out(const BJob& c, const u32x4 (&o)[4], LAS unsigned char* Tlo, LAS unsigned char* Thi) {
;     int tz = threadIdx.x; asm volatile("" : "+v"(tz));
;     const int tid = tz, w = tid >> 6, lane = tid & 63;
;     LAS unsigned char* Tw = (lane < 32) ? Tlo : Thi;
; #pragma unroll
;     for (int jn = 0; jn < 4; ++jn) { const int nl = (lane & 31) * 4 + jn;
;         *(LAS u32x4*)(Tw + nl * 128 + ((w ^ (lane & 7)) << 4)) = o[jn]; }
;     asm volatile("s_waitcnt lgkmcnt(0)" ::: "memory"); __builtin_amdgcn_s_barrier(); asm volatile("" ::: "memory");
; #pragma unroll
;     for (int p = 0; p < 4; ++p) { const int idx = tid + 512 * p, n = idx >> 3, wq = idx & 7;
;         const LAS unsigned char* Tr = (n < 128) ? Tlo : Thi;
;         const u32x4 ov = *(const LAS u32x4*)(Tr + (n & 127) * 128 + ((wq ^ ((n >> 2) & 7)) << 4));
;         const int cc = c.s0 + n; int np = cc;
;         if (c.gu) { const int bj = cc >> 11, rem = cc & 2047; np = (rem >> 7) * 256 + bj * 128 + (rem & 127); }
;         __builtin_nontemporal_store(ov, (u32x4*)(c.dst + (size_t)np * 2048 + wq * 16)); }
;     asm volatile("s_waitcnt lgkmcnt(0)" ::: "memory"); __builtin_amdgcn_s_barrier(); asm volatile("" ::: "memory");
; }
.Lbc_io_a0:
	s_lshr_b32 s28, s13, 8
	s_bfe_u32 s30, s13, 0x40004
	s_and_b32 s31, s13, 15
	s_lshl_b32 s28, s28, 23
	s_lshl_b32 s30, s30, 7
	s_add_i32 s28, s28, s30
	s_and_b32 s30, s31, 7
	s_lshl_b32 s30, s30, 20
	s_add_i32 s28, s28, s30
	s_lshr_b32 s30, s31, 3
	s_lshl_b32 s30, s30, 18
	s_add_i32 s28, s28, s30
	s_add_u32 s18, s94, s28
	s_addc_u32 s19, s95, 0
	ds_write_b128 v245, v[212:215]
	ds_write_b128 v245, v[216:219] offset:128
	ds_write_b128 v245, v[220:223] offset:256
	ds_write_b128 v245, v[224:227] offset:384
	s_waitcnt lgkmcnt(0)
	s_barrier
	ds_read_b128 v[228:231], v246
	ds_read_b128 v[232:235], v246 offset:8192
	ds_read_b128 v[236:239], v247
	ds_read_b128 v[240:243], v247 offset:8192
	s_waitcnt lgkmcnt(3)
	global_store_dwordx4 v248, v[228:231], s[18:19]
	s_add_u32 s18, s18, 0x20000
	s_addc_u32 s19, s19, 0
	s_waitcnt lgkmcnt(2)
	global_store_dwordx4 v248, v[232:235], s[18:19]
	s_add_u32 s18, s18, 0x60000
	s_addc_u32 s19, s19, 0
	s_waitcnt lgkmcnt(1)
	global_store_dwordx4 v248, v[236:239], s[18:19]
	s_add_u32 s18, s18, 0x20000
	s_addc_u32 s19, s19, 0
	s_waitcnt lgkmcnt(0)
	global_store_dwordx4 v248, v[240:243], s[18:19]
	s_barrier
	s_add_i32 s13, s13, s89
	s_cmp_ge_i32 s13, s87
	s_cbranch_scc1 .Lbc_done
.Lbc_st_b0:
	s_cmp_lg_u32 s4, 0
	s_cbranch_scc1 .Lbc_w0_b0
	s_waitcnt vmcnt(20)
	s_branch .Lbc_wd_b0

; __device__ __forceinline__ unsigned pk4_fp8_scaled(float a, float b, float c, float d) { s16x2 r = {0, 0}; r = __builtin_amdgcn_cvt_scalef32_pk_fp8_f32(r, a, b, pg8::W8_INV, false); r = __builtin_amdgcn_cvt_scalef32_pk_fp8_f32(r, c, d, pg8::W8_INV, true); return __builtin_bit_cast(unsigned, r); }
; __device__ __forceinline__ void bjob_pack(const f32x4 (&v)[16], u32x4 (&o)[4]) {
; #pragma unroll
;     for (int jn = 0; jn < 4; ++jn) {
;         o[jn].x = pk4_fp8_scaled(v[0][jn], v[1][jn], v[2][jn], v[3][jn]); o[jn].y = pk4_fp8_scaled(v[4][jn], v[5][jn], v[6][jn], v[7][jn]);
;         o[jn].z = pk4_fp8_scaled(v[8][jn], v[9][jn], v[10][jn], v[11][jn]); o[jn].w = pk4_fp8_scaled(v[12][jn], v[13][jn], v[14][jn], v[15][jn]); }
; }
; __device__ __forceinline__ void conv_share_blk(const Args& a, LAS unsigned char* lds, int blk, int G) {
;     ...
; #pragma unroll 1
;     for (;;) {
;         bjob_pack(v, o);
;         const BJob cur = cc; const bool hn = (j + nb) < j1;
;         if (hn) { cc = bjob_addr(a, j + nb); bjob_load(cc, v); }
.Lbc_wd_b0:
	v_cvt_scalef32_pk_fp8_f32 v212, v148, v152, s52
	v_cvt_scalef32_pk_fp8_f32 v213, v164, v168, s52
	v_cvt_scalef32_pk_fp8_f32 v214, v180, v184, s52
	v_cvt_scalef32_pk_fp8_f32 v215, v196, v200, s52
	v_cvt_scalef32_pk_fp8_f32 v216, v149, v153, s52
	v_cvt_scalef32_pk_fp8_f32 v217, v165, v169, s52
	v_cvt_scalef32_pk_fp8_f32 v218, v181, v185, s52
	v_cvt_scalef32_pk_fp8_f32 v219, v197, v201, s52
	v_cvt_scalef32_pk_fp8_f32 v220, v150, v154, s52
	v_cvt_scalef32_pk_fp8_f32 v221, v166, v170, s52
	v_cvt_scalef32_pk_fp8_f32 v222, v182, v186, s52
	v_cvt_scalef32_pk_fp8_f32 v223, v198, v202, s52
	v_cvt_scalef32_pk_fp8_f32 v224, v151, v155, s52
	v_cvt_scalef32_pk_fp8_f32 v225, v167, v171, s52
	v_cvt_scalef32_pk_fp8_f32 v226, v183, v187, s52
	v_cvt_scalef32_pk_fp8_f32 v227, v199, v203, s52
	v_cvt_scalef32_pk_fp8_f32 v212, v156, v160, s52 op_sel:[0,0,0,1]
	v_cvt_scalef32_pk_fp8_f32 v213, v172, v176, s52 op_sel:[0,0,0,1]
	v_cvt_scalef32_pk_fp8_f32 v214, v188, v192, s52 op_sel:[0,0,0,1]
	v_cvt_scalef32_pk_fp8_f32 v215, v204, v208, s52 op_sel:[0,0,0,1]
	v_cvt_scalef32_pk_fp8_f32 v216, v157, v161, s52 op_sel:[0,0,0,1]
	v_cvt_scalef32_pk_fp8_f32 v217, v173, v177, s52 op_sel:[0,0,0,1]
	v_cvt_scalef32_pk_fp8_f32 v218, v189, v193, s52 op_sel:[0,0,0,1]
	v_cvt_scalef32_pk_fp8_f32 v219, v205, v209, s52 op_sel:[0,0,0,1]
	v_cvt_scalef32_pk_fp8_f32 v220, v158, v162, s52 op_sel:[0,0,0,1]
	v_cvt_scalef32_pk_fp8_f32 v221, v174, v178, s52 op_sel:[0,0,0,1]
	v_cvt_scalef32_pk_fp8_f32 v222, v190, v194, s52 op_sel:[0,0,0,1]
	v_cvt_scalef32_pk_fp8_f32 v223, v206, v210, s52 op_sel:[0,0,0,1]
	v_cvt_scalef32_pk_fp8_f32 v224, v159, v163, s52 op_sel:[0,0,0,1]
	v_cvt_scalef32_pk_fp8_f32 v225, v175, v179, s52 op_sel:[0,0,0,1]
	v_cvt_scalef32_pk_fp8_f32 v226, v191, v195, s52 op_sel:[0,0,0,1]
	v_cvt_scalef32_pk_fp8_f32 v227, v207, v211, s52 op_sel:[0,0,0,1]
	s_add_i32 s33, s13, s89
	s_add_i32 s33, s33, s89
	s_cmp_ge_i32 s33, s87
	s_cbranch_scc1 .Lbc_ni_b0
	s_lshr_b32 s28, s33, 8
	s_bfe_u32 s30, s33, 0x40004
	s_and_b32 s31, s33, 15
	s_lshl_b32 s28, s28, 25
	s_lshl_b32 s30, s30, 21
	s_add_i32 s28, s28, s30
	s_lshl_b32 s31, s31, 10
	s_add_i32 s28, s28, s31
	s_lshl_b32 s30, s3, 18
	s_add_i32 s28, s28, s30
	s_add_u32 s16, s46, s28
	s_addc_u32 s17, s47, 0
	global_load_dwordx4 v[148:151], v244, s[16:17] nt
	s_add_u32 s16, s16, 0x4000
	s_addc_u32 s17, s17, 0
	global_load_dwordx4 v[152:155], v244, s[16:17] nt
	s_add_u32 s16, s16, 0x4000
	s_addc_u32 s17, s17, 0
	global_load_dwordx4 v[156:159], v244, s[16:17] nt
	s_add_u32 s16, s16, 0x4000
	s_addc_u32 s17, s17, 0
	global_load_dwordx4 v[160:163], v244, s[16:17] nt
	s_add_u32 s16, s16, 0x4000
	s_addc_u32 s17, s17, 0
	global_load_dwordx4 v[164:167], v244, s[16:17] nt
	s_add_u32 s16, s16, 0x4000
	s_addc_u32 s17, s17, 0
	global_load_dwordx4 v[168:171], v244, s[16:17] nt
	s_add_u32 s16, s16, 0x4000
	s_addc_u32 s17, s17, 0
	global_load_dwordx4 v[172:175], v244, s[16:17] nt
	s_add_u32 s16, s16, 0x4000
	s_addc_u32 s17, s17, 0
	global_load_dwordx4 v[176:179], v244, s[16:17] nt
	s_add_u32 s16, s16, 0x4000
	s_addc_u32 s17, s17, 0
	global_load_dwordx4 v[180:183], v244, s[16:17] nt
	s_add_u32 s16, s16, 0x4000
	s_addc_u32 s17, s17, 0
	global_load_dwordx4 v[184:187], v244, s[16:17] nt
	s_add_u32 s16, s16, 0x4000
	s_addc_u32 s17, s17, 0
	global_load_dwordx4 v[188:191], v244, s[16:17] nt
	s_add_u32 s16, s16, 0x4000
	s_addc_u32 s17, s17, 0
	global_load_dwordx4 v[192:195], v244, s[16:17] nt
	s_add_u32 s16, s16, 0x4000
	s_addc_u32 s17, s17, 0
	global_load_dwordx4 v[196:199], v244, s[16:17] nt
	s_add_u32 s16, s16, 0x4000
	s_addc_u32 s17, s17, 0
	global_load_dwordx4 v[200:203], v244, s[16:17] nt
	s_add_u32 s16, s16, 0x4000
	s_addc_u32 s17, s17, 0
	global_load_dwordx4 v[204:207], v244, s[16:17] nt
	s_add_u32 s16, s16, 0x4000
	s_addc_u32 s17, s17, 0
	global_load_dwordx4 v[208:211], v244, s[16:17] nt
	s_branch .Lbc_io_b0

; __device__ __forceinline__ void conv_share_blk(const Args& a, LAS unsigned char* lds, int blk, int G) {
;     ...
; #pragma unroll 1
;     for (;;) {
;         bjob_pack(v, o);
;         const BJob cur = cc; const bool hn = (j + nb) < j1;
;         if (hn) { cc = bjob_addr(a, j + nb); bjob_load(cc, v); }
;         bjob_out(cur, o, Tlo, Thi);
;         if (!hn) break;
;         j += nb;
;     }
.Lbc_loop:
.Lbc_st_a:
	s_cmp_lg_u32 s4, 0
	s_cbranch_scc1 .Lbc_w0_a
	s_waitcnt vmcnt(24)
	s_branch .Lbc_wd_a

; __device__ __forceinline__ void conv_share_blk(const Args& a, LAS unsigned char* lds, int blk, int G) {
;     ...
; #pragma unroll 1
;     for (;;) {
;         bjob_pack(v, o);
;         const BJob cur = cc; const bool hn = (j + nb) < j1;
;         if (hn) { cc = bjob_addr(a, j + nb); bjob_load(cc, v); }
;         bjob_out(cur, o, Tlo, Thi);
;         if (!hn) break;
;         j += nb;
;     }
.Lbc_st_b:
	s_cmp_lg_u32 s4, 0
	s_cbranch_scc1 .Lbc_w0_b
	s_waitcnt vmcnt(24)
	s_branch .Lbc_wd_b

; #define LAS __attribute__((address_space(3)))
; __device__ __forceinline__ void bjob_out(const BJob& c, const u32x4 (&o)[4], LAS unsigned char* Tlo, LAS unsigned char* Thi) {
;     int tz = threadIdx.x; asm volatile("" : "+v"(tz));
;     const int tid = tz, w = tid >> 6, lane = tid & 63;
;     LAS unsigned char* Tw = (lane < 32) ? Tlo : Thi;
; #pragma unroll
;     for (int jn = 0; jn < 4; ++jn) { const int nl = (lane & 31) * 4 + jn;
;         *(LAS u32x4*)(Tw + nl * 128 + ((w ^ (lane & 7)) << 4)) = o[jn]; }
;     asm volatile("s_waitcnt lgkmcnt(0)" ::: "memory"); __builtin_amdgcn_s_barrier(); asm volatile("" ::: "memory");
; #pragma unroll
;     for (int p = 0; p < 4; ++p) { const int idx = tid + 512 * p, n = idx >> 3, wq = idx & 7;
;         const LAS unsigned char* Tr = (n < 128) ? Tlo : Thi;
;         const u32x4 ov = *(const LAS u32x4*)(Tr + (n & 127) * 128 + ((wq ^ ((n >> 2) & 7)) << 4));
;         const int cc = c.s0 + n; int np = cc;
;         if (c.gu) { const int bj = cc >> 11, rem = cc & 2047; np = (rem >> 7) * 256 + bj * 128 + (rem & 127); }
;         __builtin_nontemporal_store(ov, (u32x4*)(c.dst + (size_t)np * 2048 + wq * 16)); }
;     asm volatile("s_waitcnt lgkmcnt(0)" ::: "memory"); __builtin_amdgcn_s_barrier(); asm volatile("" ::: "memory");
; }
.Lbc_io_b:
	s_lshr_b32 s28, s13, 8
	s_bfe_u32 s30, s13, 0x40004
	s_and_b32 s31, s13, 15
	s_lshl_b32 s28, s28, 23
	s_lshl_b32 s30, s30, 7
	s_add_i32 s28, s28, s30
	s_and_b32 s30, s31, 7
	s_lshl_b32 s30, s30, 20
	s_add_i32 s28, s28, s30
	s_lshr_b32 s30, s31, 3
	s_lshl_b32 s30, s30, 18
	s_add_i32 s28, s28, s30
	s_add_u32 s18, s94, s28
	s_addc_u32 s19, s95, 0
	ds_write_b128 v245, v[212:215]
	ds_write_b128 v245, v[216:219] offset:128
	ds_write_b128 v245, v[220:223] offset:256
	ds_write_b128 v245, v[224:227] offset:384
	s_waitcnt lgkmcnt(0)
	s_barrier
	ds_read_b128 v[228:231], v246
	ds_read_b128 v[232:235], v246 offset:8192
	ds_read_b128 v[236:239], v247
	ds_read_b128 v[240:243], v247 offset:8192
	s_waitcnt lgkmcnt(3)
	global_store_dwordx4 v248, v[228:231], s[18:19]
	s_add_u32 s18, s18, 0x20000
	s_addc_u32 s19, s19, 0
	s_waitcnt lgkmcnt(2)
	global_store_dwordx4 v248, v[232:235], s[18:19]
	s_add_u32 s18, s18, 0x60000
	s_addc_u32 s19, s19, 0
	s_waitcnt lgkmcnt(1)
	global_store_dwordx4 v248, v[236:239], s[18:19]
	s_add_u32 s18, s18, 0x20000
	s_addc_u32 s19, s19, 0
	s_waitcnt lgkmcnt(0)
	global_store_dwordx4 v248, v[240:243], s[18:19]
	s_barrier
	s_add_i32 s13, s13, s89
	s_cmp_ge_i32 s13, s87
	s_cbranch_scc1 .Lbc_done
	s_branch .Lbc_loop
.Lbc_done:
	s_cmp_ge_u32 s3, 4
	s_cbranch_scc0 .Lbc_nob1
	s_barrier
.Lbc_nob1:
	s_branch .LBB0_170

; #define PG8_ROWS(x0, uidx) do { ro[x0] = (unsigned)g.rowtab[(uidx) * 256 + Rl + 64 * (x0)]; ro[(x0) + 1] = (unsigned)g.rowtab[(uidx) * 256 + Rl + 64 * (x0) + 64]; } while (0)
; #define PG8_STAGE(bufoff, gbase, voff) do { _Pragma("unroll") for (int _i = 0; _i < 2; ++_i) \
;         __builtin_amdgcn_global_load_lds((const unsigned*)(sbase((const char*)(gbase) + _i * pstep) + (voff)), (LAS unsigned*)(lds + (bufoff) + ldsw + _i * 8192), 16, 0, 0); } while (0)
; #define PG8_LDA(dst, b, h) do { _Pragma("unroll") for (int m = 0; m < 4; ++m) { \
;         if constexpr (FP8) dst##8[m] = ld32(lds + PG8_SA(b, h) + aoff0 + m * 2048); \
;         else { dst[m][0] = *(const LAS bf16x8*)(lds + PG8_SA(b, h) + aoff0 + m * 2048); dst[m][1] = *(const LAS bf16x8*)(lds + PG8_SA(b, h) + aoff0 + m * 2048 + 1024); } } } while (0)
; #define PG8_LDB(dst, b, h) do { _Pragma("unroll") for (int n = 0; n < 2; ++n) { \
;         if constexpr (FP8) dst##8[n] = ld32(lds + PG8_SB(b, h) + boff0 + n * 2048); \
;         else { dst[n][0] = *(const LAS bf16x8*)(lds + PG8_SB(b, h) + boff0 + n * 2048); dst[n][1] = *(const LAS bf16x8*)(lds + PG8_SB(b, h) + boff0 + n * 2048 + 1024); } } } while (0)
; #define PG8_WAIT_V(n) asm volatile("s_waitcnt vmcnt(" #n ")" ::: "memory")
; template <bool FP8, bool GATHER, class Epi, class Sched>
; __device__ __forceinline__ void gemm_phase(LAS unsigned char* lds, const Gemm g, const Sched& S, const Epi& E) {
;     ...
;             PG8_LDB(B0, 0, 0); PG8_SCHED; PG8_LDA(At, 0, 0); PG8_STAGEA(PG8_SA(1, 1), false, 1, k1);
;             if constexpr (GATHER) { if (last && has_next) PG8_ROWS(2, ui + 1); }
;             PG8_WAIT_V(10); PG8_WAIT_L(8); PG8_BAR; PG8_WAIT_L(0); PG8_MMA(0, 0, At, B0); PG8_BAR; PG8_SCHED;
;             PG8_LDB(B1, 0, 1); PG8_STAGE(PG8_SB(0, 0), b2, voffB);
;             PG8_WAIT_V(10); PG8_BAR; PG8_WAIT_L(0); PG8_MMA(0, 1, At, B1); PG8_BAR;
;             PG8_LDA(At, 0, 1); PG8_STAGEA(PG8_SA(0, 0), last, 0, k2);
;             PG8_BAR; PG8_WAIT_L(0); if (cfull) PG8_MMA(1, 0, At, B0); PG8_BAR; PG8_SCHED;
;             PG8_STAGE(PG8_SB(0, 1), b2 + hstep, voffB);
;             PG8_WAIT_V(10); PG8_BAR; if (cfull) PG8_MMA(1, 1, At, B1); PG8_BAR;
;             PG8_LDB(B0, 1, 0); PG8_SCHED; PG8_LDA(At, 1, 0); PG8_STAGEA(PG8_SA(0, 1), last, 1, k2);
;             PG8_WAIT_V(10); PG8_WAIT_L(8); PG8_BAR; PG8_WAIT_L(0); PG8_MMA(0, 0, At, B0); PG8_BAR; PG8_SCHED;
.LBB0_174:
	ds_read_b128 v[140:143], v145
	ds_read_b128 v[148:151], v145 offset:1024
	ds_read_b128 v[152:155], v145 offset:2048
	ds_read_b128 v[156:159], v145 offset:3072
	s_add_u32 s23, s54, s58
	s_addc_u32 s96, s55, s59
	s_cmp_eq_u32 s21, 28
	s_cselect_b64 s[62:63], -1, 0
	s_and_b64 s[60:61], s[62:63], exec
	s_cselect_b32 vcc_lo, 0, s58
	s_cselect_b32 s61, s7, s96
	s_cselect_b32 s60, s12, s23
	s_add_u32 s23, s56, s58
	s_addc_u32 vcc_hi, s57, s59
	s_add_u32 s96, s23, 0x7ff80
	s_addc_u32 s97, vcc_hi, 0
	ds_read_b128 v[160:163], v146
	ds_read_b128 v[164:167], v146 offset:1024
	ds_read_b128 v[168:171], v146 offset:2048
	ds_read_b128 v[172:175], v146 offset:3072
	ds_read_b128 v[176:179], v146 offset:4096
	ds_read_b128 v[180:183], v146 offset:5120
	ds_read_b128 v[184:187], v146 offset:6144
	ds_read_b128 v[188:191], v146 offset:7168
	s_add_i32 m0, s78, 0xc000
	v_lshl_add_u64 v[192:193], s[96:97], 0, v[132:133]
	s_add_u32 s96, s23, 0xbff80
	s_addc_u32 s97, vcc_hi, 0
	global_load_lds_dwordx4 v[192:193], off
	s_add_i32 m0, s78, 0xe000
	v_lshl_add_u64 v[192:193], s[96:97], 0, v[132:133]
	global_load_lds_dwordx4 v[192:193], off
	s_waitcnt vmcnt(10)
	s_waitcnt lgkmcnt(8)
	s_barrier
	s_waitcnt lgkmcnt(0)
	s_setprio 1
	s_waitcnt lgkmcnt(0)
	v_mfma_f32_16x16x32_bf16 v[126:129], v[140:143], v[160:163], v[126:129]
	v_mfma_f32_16x16x32_bf16 v[122:125], v[152:155], v[160:163], v[122:125]
	v_mfma_f32_16x16x32_bf16 v[114:117], v[140:143], v[168:171], v[114:117]
	v_mfma_f32_16x16x32_bf16 v[106:109], v[152:155], v[168:171], v[106:109]
	v_mfma_f32_16x16x32_bf16 v[98:101], v[140:143], v[176:179], v[98:101]
	v_mfma_f32_16x16x32_bf16 v[90:93], v[152:155], v[176:179], v[90:93]
	v_mfma_f32_16x16x32_bf16 v[82:85], v[140:143], v[184:187], v[82:85]
	v_mfma_f32_16x16x32_bf16 v[74:77], v[152:155], v[184:187], v[74:77]
	v_mfma_f32_16x16x32_bf16 v[126:129], v[148:151], v[164:167], v[126:129]
	v_mfma_f32_16x16x32_bf16 v[122:125], v[156:159], v[164:167], v[122:125]
	v_mfma_f32_16x16x32_bf16 v[114:117], v[148:151], v[172:175], v[114:117]
	v_mfma_f32_16x16x32_bf16 v[106:109], v[156:159], v[172:175], v[106:109]
	v_mfma_f32_16x16x32_bf16 v[98:101], v[148:151], v[180:183], v[98:101]
	v_mfma_f32_16x16x32_bf16 v[90:93], v[156:159], v[180:183], v[90:93]
	v_mfma_f32_16x16x32_bf16 v[82:85], v[148:151], v[188:191], v[82:85]
	v_mfma_f32_16x16x32_bf16 v[74:77], v[156:159], v[188:191], v[74:77]
	s_setprio 0
	s_barrier
	s_mov_b64 s[96:97], s[60:61]
	ds_read_b128 v[192:195], v147
	ds_read_b128 v[196:199], v147 offset:1024
	ds_read_b128 v[200:203], v147 offset:2048
	ds_read_b128 v[204:207], v147 offset:3072
	s_add_i32 s23, s29, s67
	v_lshl_add_u64 v[208:209], s[96:97], 0, v[130:131]
	s_add_u32 s96, s60, 0x40000
	s_mov_b32 m0, s23
	s_addc_u32 s97, s61, 0
	global_load_lds_dwordx4 v[208:209], off
	s_add_i32 m0, s23, 0x2000
	v_lshl_add_u64 v[208:209], s[96:97], 0, v[130:131]
	global_load_lds_dwordx4 v[208:209], off
	s_waitcnt vmcnt(10)
	s_barrier
	s_waitcnt lgkmcnt(0)
	s_setprio 1
	s_waitcnt lgkmcnt(0)
	v_mfma_f32_16x16x32_bf16 v[118:121], v[192:195], v[160:163], v[118:121]
	v_mfma_f32_16x16x32_bf16 v[110:113], v[200:203], v[160:163], v[110:113]
	v_mfma_f32_16x16x32_bf16 v[102:105], v[192:195], v[168:171], v[102:105]
	v_mfma_f32_16x16x32_bf16 v[94:97], v[200:203], v[168:171], v[94:97]
	v_mfma_f32_16x16x32_bf16 v[86:89], v[192:195], v[176:179], v[86:89]
	v_mfma_f32_16x16x32_bf16 v[78:81], v[200:203], v[176:179], v[78:81]
	v_mfma_f32_16x16x32_bf16 v[70:73], v[192:195], v[184:187], v[70:73]
	v_mfma_f32_16x16x32_bf16 v[66:69], v[200:203], v[184:187], v[66:69]
	v_mfma_f32_16x16x32_bf16 v[118:121], v[196:199], v[164:167], v[118:121]
	v_mfma_f32_16x16x32_bf16 v[110:113], v[204:207], v[164:167], v[110:113]
	v_mfma_f32_16x16x32_bf16 v[102:105], v[196:199], v[172:175], v[102:105]
	v_mfma_f32_16x16x32_bf16 v[94:97], v[204:207], v[172:175], v[94:97]
	v_mfma_f32_16x16x32_bf16 v[86:89], v[196:199], v[180:183], v[86:89]
	v_mfma_f32_16x16x32_bf16 v[78:81], v[204:207], v[180:183], v[78:81]
	v_mfma_f32_16x16x32_bf16 v[70:73], v[196:199], v[188:191], v[70:73]
	v_mfma_f32_16x16x32_bf16 v[66:69], v[204:207], v[188:191], v[66:69]
	s_setprio 0
	s_and_b64 s[62:63], s[10:11], s[62:63]
	s_and_b64 s[62:63], s[62:63], exec
	s_cselect_b32 s62, s34, s56
	s_cselect_b32 s23, s35, s57
	s_add_u32 s62, s62, vcc_lo
	s_addc_u32 s63, s23, 0
	s_mov_b64 s[96:97], s[62:63]
	s_barrier
	ds_read_b128 v[160:163], v146 offset:16384
	ds_read_b128 v[164:167], v146 offset:17408
	ds_read_b128 v[168:171], v146 offset:18432
	ds_read_b128 v[172:175], v146 offset:19456
	ds_read_b128 v[176:179], v146 offset:20480
	ds_read_b128 v[180:183], v146 offset:21504
	ds_read_b128 v[184:187], v146 offset:22528
	ds_read_b128 v[188:191], v146 offset:23552
	s_mov_b32 m0, s78
	v_lshl_add_u64 v[208:209], s[96:97], 0, v[132:133]
	s_add_u32 s96, s62, 0x40000
	s_addc_u32 s97, s63, 0
	global_load_lds_dwordx4 v[208:209], off
	s_mov_b32 m0, s79
	v_lshl_add_u64 v[208:209], s[96:97], 0, v[132:133]
	global_load_lds_dwordx4 v[208:209], off
	s_barrier
	s_waitcnt lgkmcnt(0)
	s_setprio 1
	s_waitcnt lgkmcnt(0)
	v_mfma_f32_16x16x32_bf16 v[62:65], v[140:143], v[160:163], v[62:65]
	v_mfma_f32_16x16x32_bf16 v[58:61], v[152:155], v[160:163], v[58:61]
	v_mfma_f32_16x16x32_bf16 v[54:57], v[140:143], v[168:171], v[54:57]
	v_mfma_f32_16x16x32_bf16 v[46:49], v[152:155], v[168:171], v[46:49]
	v_mfma_f32_16x16x32_bf16 v[38:41], v[140:143], v[176:179], v[38:41]
	v_mfma_f32_16x16x32_bf16 v[30:33], v[152:155], v[176:179], v[30:33]
	v_mfma_f32_16x16x32_bf16 v[22:25], v[140:143], v[184:187], v[22:25]
	v_mfma_f32_16x16x32_bf16 v[14:17], v[152:155], v[184:187], v[14:17]
	v_mfma_f32_16x16x32_bf16 v[62:65], v[148:151], v[164:167], v[62:65]
	v_mfma_f32_16x16x32_bf16 v[58:61], v[156:159], v[164:167], v[58:61]
	v_mfma_f32_16x16x32_bf16 v[54:57], v[148:151], v[172:175], v[54:57]
	v_mfma_f32_16x16x32_bf16 v[46:49], v[156:159], v[172:175], v[46:49]
	v_mfma_f32_16x16x32_bf16 v[38:41], v[148:151], v[180:183], v[38:41]
	v_mfma_f32_16x16x32_bf16 v[30:33], v[156:159], v[180:183], v[30:33]
	v_mfma_f32_16x16x32_bf16 v[22:25], v[148:151], v[188:191], v[22:25]
	v_mfma_f32_16x16x32_bf16 v[14:17], v[156:159], v[188:191], v[14:17]
	s_setprio 0
	s_barrier
; #define PG8_STAGE(bufoff, gbase, voff) do { _Pragma("unroll") for (int _i = 0; _i < 2; ++_i) \
;         __builtin_amdgcn_global_load_lds((const unsigned*)(sbase((const char*)(gbase) + _i * pstep) + (voff)), (LAS unsigned*)(lds + (bufoff) + ldsw + _i * 8192), 16, 0, 0); } while (0)
; #define PG8_LDA(dst, b, h) do { _Pragma("unroll") for (int m = 0; m < 4; ++m) { \
;         if constexpr (FP8) dst##8[m] = ld32(lds + PG8_SA(b, h) + aoff0 + m * 2048); \
;         else { dst[m][0] = *(const LAS bf16x8*)(lds + PG8_SA(b, h) + aoff0 + m * 2048); dst[m][1] = *(const LAS bf16x8*)(lds + PG8_SA(b, h) + aoff0 + m * 2048 + 1024); } } } while (0)
; #define PG8_LDB(dst, b, h) do { _Pragma("unroll") for (int n = 0; n < 2; ++n) { \
;         if constexpr (FP8) dst##8[n] = ld32(lds + PG8_SB(b, h) + boff0 + n * 2048); \
;         else { dst[n][0] = *(const LAS bf16x8*)(lds + PG8_SB(b, h) + boff0 + n * 2048); dst[n][1] = *(const LAS bf16x8*)(lds + PG8_SB(b, h) + boff0 + n * 2048 + 1024); } } } while (0)
; #define PG8_WAIT_V(n) asm volatile("s_waitcnt vmcnt(" #n ")" ::: "memory")
; #define PG8_WAIT_L(n) asm volatile("s_waitcnt lgkmcnt(" #n ")" ::: "memory")
; #define PG8_BAR __builtin_amdgcn_s_barrier()
; template <bool FP8, bool GATHER, class Epi, class Sched>
; __device__ __forceinline__ void gemm_phase(LAS unsigned char* lds, const Gemm g, const Sched& S, const Epi& E) {
;     ...
;             PG8_LDB(B1, 0, 1); PG8_STAGE(PG8_SB(0, 0), b2, voffB);
;             PG8_WAIT_V(10); PG8_BAR; PG8_WAIT_L(0); PG8_MMA(0, 1, At, B1); PG8_BAR;
;             PG8_LDA(At, 0, 1); PG8_STAGEA(PG8_SA(0, 0), last, 0, k2);
;             PG8_BAR; PG8_WAIT_L(0); if (cfull) PG8_MMA(1, 0, At, B0); PG8_BAR; PG8_SCHED;
;             PG8_STAGE(PG8_SB(0, 1), b2 + hstep, voffB);
;             PG8_WAIT_V(10); PG8_BAR; if (cfull) PG8_MMA(1, 1, At, B1); PG8_BAR;
;             PG8_LDB(B0, 1, 0); PG8_SCHED; PG8_LDA(At, 1, 0); PG8_STAGEA(PG8_SA(0, 1), last, 1, k2);
;             PG8_WAIT_V(10); PG8_WAIT_L(8); PG8_BAR; PG8_WAIT_L(0); PG8_MMA(0, 0, At, B0); PG8_BAR; PG8_SCHED;
;             PG8_LDB(B1, 1, 1); PG8_STAGE(PG8_SB(1, 0), b3, voffB);
;             PG8_WAIT_V(10); PG8_BAR; PG8_WAIT_L(0); PG8_MMA(0, 1, At, B1); PG8_BAR;
;             PG8_LDA(At, 1, 1); PG8_STAGEA(PG8_SA(1, 0), last, 0, k3);
;             PG8_BAR; PG8_WAIT_L(0); if (cfull) PG8_MMA(1, 0, At, B0); PG8_BAR; PG8_SCHED;
	s_add_u32 s96, s60, 0x80000
	s_addc_u32 s97, s61, 0
	s_add_i32 s23, s24, s67
	v_lshl_add_u64 v[140:141], s[96:97], 0, v[130:131]
	s_add_u32 s96, s60, 0xc0000
	s_mov_b32 m0, s23
	s_addc_u32 s97, s61, 0
	global_load_lds_dwordx4 v[140:141], off
	s_add_i32 m0, s23, 0x2000
	v_lshl_add_u64 v[140:141], s[96:97], 0, v[130:131]
	global_load_lds_dwordx4 v[140:141], off
	s_waitcnt vmcnt(10)
	s_barrier
	s_setprio 1
	v_mfma_f32_16x16x32_bf16 v[50:53], v[192:195], v[160:163], v[50:53]
	v_mfma_f32_16x16x32_bf16 v[42:45], v[200:203], v[160:163], v[42:45]
	v_mfma_f32_16x16x32_bf16 v[34:37], v[192:195], v[168:171], v[34:37]
	v_mfma_f32_16x16x32_bf16 v[26:29], v[200:203], v[168:171], v[26:29]
	v_mfma_f32_16x16x32_bf16 v[18:21], v[192:195], v[176:179], v[18:21]
	v_mfma_f32_16x16x32_bf16 v[10:13], v[200:203], v[176:179], v[10:13]
	v_mfma_f32_16x16x32_bf16 v[6:9], v[192:195], v[184:187], v[6:9]
	v_mfma_f32_16x16x32_bf16 v[2:5], v[200:203], v[184:187], v[2:5]
	v_mfma_f32_16x16x32_bf16 v[50:53], v[196:199], v[164:167], v[50:53]
	v_mfma_f32_16x16x32_bf16 v[42:45], v[204:207], v[164:167], v[42:45]
	v_mfma_f32_16x16x32_bf16 v[34:37], v[196:199], v[172:175], v[34:37]
	v_mfma_f32_16x16x32_bf16 v[26:29], v[204:207], v[172:175], v[26:29]
	v_mfma_f32_16x16x32_bf16 v[18:21], v[196:199], v[180:183], v[18:21]
	v_mfma_f32_16x16x32_bf16 v[10:13], v[204:207], v[180:183], v[10:13]
	v_mfma_f32_16x16x32_bf16 v[6:9], v[196:199], v[188:191], v[6:9]
	v_mfma_f32_16x16x32_bf16 v[2:5], v[204:207], v[188:191], v[2:5]
	s_setprio 0
	s_add_i32 s23, 0, 0x18000
	v_add_u32_e32 v134, s23, v1
	s_barrier
	ds_read_b128 v[140:143], v134
	ds_read_b128 v[148:151], v134 offset:1024
	ds_read_b128 v[152:155], v134 offset:2048
	ds_read_b128 v[156:159], v134 offset:3072
	s_add_u32 s96, s62, 0x80000
	s_addc_u32 s97, s63, 0
	ds_read_b128 v[160:163], v146 offset:32768
	ds_read_b128 v[164:167], v146 offset:33792
	ds_read_b128 v[168:171], v146 offset:34816
	ds_read_b128 v[172:175], v146 offset:35840
	ds_read_b128 v[176:179], v146 offset:36864
	ds_read_b128 v[180:183], v146 offset:37888
	ds_read_b128 v[184:187], v146 offset:38912
	ds_read_b128 v[188:191], v146 offset:39936
	s_mov_b32 m0, s80
	v_lshl_add_u64 v[192:193], s[96:97], 0, v[132:133]
	s_add_u32 s96, s62, 0xc0000
	s_addc_u32 s97, s63, 0
	global_load_lds_dwordx4 v[192:193], off
	s_mov_b32 m0, s81
	v_lshl_add_u64 v[192:193], s[96:97], 0, v[132:133]
	global_load_lds_dwordx4 v[192:193], off
	s_waitcnt vmcnt(10)
	s_waitcnt lgkmcnt(8)
	s_barrier
	s_waitcnt lgkmcnt(0)
	s_setprio 1
	s_waitcnt lgkmcnt(0)
	v_mfma_f32_16x16x32_bf16 v[126:129], v[140:143], v[160:163], v[126:129]
	v_mfma_f32_16x16x32_bf16 v[122:125], v[152:155], v[160:163], v[122:125]
	v_mfma_f32_16x16x32_bf16 v[114:117], v[140:143], v[168:171], v[114:117]
	v_mfma_f32_16x16x32_bf16 v[106:109], v[152:155], v[168:171], v[106:109]
	v_mfma_f32_16x16x32_bf16 v[98:101], v[140:143], v[176:179], v[98:101]
	v_mfma_f32_16x16x32_bf16 v[90:93], v[152:155], v[176:179], v[90:93]
	v_mfma_f32_16x16x32_bf16 v[82:85], v[140:143], v[184:187], v[82:85]
	v_mfma_f32_16x16x32_bf16 v[74:77], v[152:155], v[184:187], v[74:77]
	v_mfma_f32_16x16x32_bf16 v[126:129], v[148:151], v[164:167], v[126:129]
	v_mfma_f32_16x16x32_bf16 v[122:125], v[156:159], v[164:167], v[122:125]
	v_mfma_f32_16x16x32_bf16 v[114:117], v[148:151], v[172:175], v[114:117]
	v_mfma_f32_16x16x32_bf16 v[106:109], v[156:159], v[172:175], v[106:109]
	v_mfma_f32_16x16x32_bf16 v[98:101], v[148:151], v[180:183], v[98:101]
	v_mfma_f32_16x16x32_bf16 v[90:93], v[156:159], v[180:183], v[90:93]
	v_mfma_f32_16x16x32_bf16 v[82:85], v[148:151], v[188:191], v[82:85]
	v_mfma_f32_16x16x32_bf16 v[74:77], v[156:159], v[188:191], v[74:77]
	s_setprio 0
	s_barrier
	s_add_i32 vcc_lo, 0, 0x1c000
	s_add_u32 s96, s60, 0x80
	v_add_u32_e32 v134, vcc_lo, v1
	s_addc_u32 s97, s61, 0
	ds_read_b128 v[192:195], v134
	ds_read_b128 v[196:199], v134 offset:1024
	ds_read_b128 v[200:203], v134 offset:2048
	ds_read_b128 v[204:207], v134 offset:3072
	s_add_i32 s23, s23, s67
	v_lshl_add_u64 v[208:209], s[96:97], 0, v[130:131]
	s_add_u32 s96, s60, 0x40080
	s_mov_b32 m0, s23
	s_addc_u32 s97, s61, 0
	global_load_lds_dwordx4 v[208:209], off
	s_add_i32 m0, s23, 0x2000
	v_lshl_add_u64 v[208:209], s[96:97], 0, v[130:131]
	global_load_lds_dwordx4 v[208:209], off
	s_waitcnt vmcnt(10)
	s_barrier
	s_waitcnt lgkmcnt(0)
	s_setprio 1
	s_waitcnt lgkmcnt(0)
	v_mfma_f32_16x16x32_bf16 v[118:121], v[192:195], v[160:163], v[118:121]
	v_mfma_f32_16x16x32_bf16 v[110:113], v[200:203], v[160:163], v[110:113]
	v_mfma_f32_16x16x32_bf16 v[102:105], v[192:195], v[168:171], v[102:105]
	v_mfma_f32_16x16x32_bf16 v[94:97], v[200:203], v[168:171], v[94:97]
	v_mfma_f32_16x16x32_bf16 v[86:89], v[192:195], v[176:179], v[86:89]
	v_mfma_f32_16x16x32_bf16 v[78:81], v[200:203], v[176:179], v[78:81]
	v_mfma_f32_16x16x32_bf16 v[70:73], v[192:195], v[184:187], v[70:73]
	v_mfma_f32_16x16x32_bf16 v[66:69], v[200:203], v[184:187], v[66:69]
	v_mfma_f32_16x16x32_bf16 v[118:121], v[196:199], v[164:167], v[118:121]
	v_mfma_f32_16x16x32_bf16 v[110:113], v[204:207], v[164:167], v[110:113]
	v_mfma_f32_16x16x32_bf16 v[102:105], v[196:199], v[172:175], v[102:105]
	v_mfma_f32_16x16x32_bf16 v[94:97], v[204:207], v[172:175], v[94:97]
	v_mfma_f32_16x16x32_bf16 v[86:89], v[196:199], v[180:183], v[86:89]
	v_mfma_f32_16x16x32_bf16 v[78:81], v[204:207], v[180:183], v[78:81]
	v_mfma_f32_16x16x32_bf16 v[70:73], v[196:199], v[188:191], v[70:73]
	v_mfma_f32_16x16x32_bf16 v[66:69], v[204:207], v[188:191], v[66:69]
	s_setprio 0
	s_add_u32 s96, s62, 0x80
	s_addc_u32 s97, s63, 0
	s_add_u32 s62, s62, 0x40080
	s_mov_b32 m0, s84
	s_barrier
; #define PG8_STAGE(bufoff, gbase, voff) do { _Pragma("unroll") for (int _i = 0; _i < 2; ++_i) \
;         __builtin_amdgcn_global_load_lds((const unsigned*)(sbase((const char*)(gbase) + _i * pstep) + (voff)), (LAS unsigned*)(lds + (bufoff) + ldsw + _i * 8192), 16, 0, 0); } while (0)
; #define PG8_LDA(dst, b, h) do { _Pragma("unroll") for (int m = 0; m < 4; ++m) { \
;         if constexpr (FP8) dst##8[m] = ld32(lds + PG8_SA(b, h) + aoff0 + m * 2048); \
;         else { dst[m][0] = *(const LAS bf16x8*)(lds + PG8_SA(b, h) + aoff0 + m * 2048); dst[m][1] = *(const LAS bf16x8*)(lds + PG8_SA(b, h) + aoff0 + m * 2048 + 1024); } } } while (0)
; #define PG8_LDB(dst, b, h) do { _Pragma("unroll") for (int n = 0; n < 2; ++n) { \
;         if constexpr (FP8) dst##8[n] = ld32(lds + PG8_SB(b, h) + boff0 + n * 2048); \
;         else { dst[n][0] = *(const LAS bf16x8*)(lds + PG8_SB(b, h) + boff0 + n * 2048); dst[n][1] = *(const LAS bf16x8*)(lds + PG8_SB(b, h) + boff0 + n * 2048 + 1024); } } } while (0)
; #define PG8_WAIT_V(n) asm volatile("s_waitcnt vmcnt(" #n ")" ::: "memory")
; #define PG8_WAIT_L(n) asm volatile("s_waitcnt lgkmcnt(" #n ")" ::: "memory")
; #define PG8_BAR __builtin_amdgcn_s_barrier()
; #define PG8_SCHED __builtin_amdgcn_sched_barrier(0)
; template <bool FP8, bool GATHER, class Epi, class Sched>
; __device__ __forceinline__ void gemm_phase(LAS unsigned char* lds, const Gemm g, const Sched& S, const Epi& E) {
;     ...
;             PG8_LDB(B1, 1, 1); PG8_STAGE(PG8_SB(1, 0), b3, voffB);
;             PG8_WAIT_V(10); PG8_BAR; PG8_WAIT_L(0); PG8_MMA(0, 1, At, B1); PG8_BAR;
;             PG8_LDA(At, 1, 1); PG8_STAGEA(PG8_SA(1, 0), last, 0, k3);
;             PG8_BAR; PG8_WAIT_L(0); if (cfull) PG8_MMA(1, 0, At, B0); PG8_BAR; PG8_SCHED;
;             PG8_STAGE(PG8_SB(1, 1), b3 + hstep, voffB);
;             PG8_WAIT_V(10); PG8_BAR; if (cfull) PG8_MMA(1, 1, At, B1); PG8_BAR;
	ds_read_b128 v[160:163], v146 offset:49152
	ds_read_b128 v[164:167], v146 offset:50176
	ds_read_b128 v[168:171], v146 offset:51200
	ds_read_b128 v[172:175], v146 offset:52224
	ds_read_b128 v[176:179], v146 offset:53248
	ds_read_b128 v[180:183], v146 offset:54272
	ds_read_b128 v[184:187], v146 offset:55296
	ds_read_b128 v[188:191], v146 offset:56320
	s_addc_u32 s63, s63, 0
	v_lshl_add_u64 v[208:209], s[96:97], 0, v[132:133]
	global_load_lds_dwordx4 v[208:209], off
	s_mov_b32 m0, s85
	v_lshl_add_u64 v[208:209], s[62:63], 0, v[132:133]
	global_load_lds_dwordx4 v[208:209], off
	s_barrier
	s_waitcnt lgkmcnt(0)
	s_setprio 1
	s_waitcnt lgkmcnt(0)
	v_mfma_f32_16x16x32_bf16 v[62:65], v[140:143], v[160:163], v[62:65]
	v_mfma_f32_16x16x32_bf16 v[58:61], v[152:155], v[160:163], v[58:61]
	v_mfma_f32_16x16x32_bf16 v[54:57], v[140:143], v[168:171], v[54:57]
	v_mfma_f32_16x16x32_bf16 v[46:49], v[152:155], v[168:171], v[46:49]
	v_mfma_f32_16x16x32_bf16 v[38:41], v[140:143], v[176:179], v[38:41]
	v_mfma_f32_16x16x32_bf16 v[30:33], v[152:155], v[176:179], v[30:33]
	v_mfma_f32_16x16x32_bf16 v[22:25], v[140:143], v[184:187], v[22:25]
	v_mfma_f32_16x16x32_bf16 v[14:17], v[152:155], v[184:187], v[14:17]
	v_mfma_f32_16x16x32_bf16 v[62:65], v[148:151], v[164:167], v[62:65]
	v_mfma_f32_16x16x32_bf16 v[58:61], v[156:159], v[164:167], v[58:61]
	v_mfma_f32_16x16x32_bf16 v[54:57], v[148:151], v[172:175], v[54:57]
	v_mfma_f32_16x16x32_bf16 v[46:49], v[156:159], v[172:175], v[46:49]
	v_mfma_f32_16x16x32_bf16 v[38:41], v[148:151], v[180:183], v[38:41]
	v_mfma_f32_16x16x32_bf16 v[30:33], v[156:159], v[180:183], v[30:33]
	v_mfma_f32_16x16x32_bf16 v[22:25], v[148:151], v[188:191], v[22:25]
	v_mfma_f32_16x16x32_bf16 v[14:17], v[156:159], v[188:191], v[14:17]
	s_setprio 0
	s_barrier
	s_add_u32 s62, s60, 0x80080
	s_addc_u32 s63, s61, 0
	s_add_i32 s23, vcc_lo, s67
	s_add_u32 s60, s60, 0xc0080
	s_mov_b32 m0, s23
	v_lshl_add_u64 v[140:141], s[62:63], 0, v[130:131]
	s_addc_u32 s61, s61, 0
	global_load_lds_dwordx4 v[140:141], off
	s_add_i32 m0, s23, 0x2000
	v_lshl_add_u64 v[140:141], s[60:61], 0, v[130:131]
	global_load_lds_dwordx4 v[140:141], off
	s_waitcnt vmcnt(10)
	s_barrier
	s_setprio 1
	v_mfma_f32_16x16x32_bf16 v[50:53], v[192:195], v[160:163], v[50:53]
	v_mfma_f32_16x16x32_bf16 v[42:45], v[200:203], v[160:163], v[42:45]
	v_mfma_f32_16x16x32_bf16 v[34:37], v[192:195], v[168:171], v[34:37]
	v_mfma_f32_16x16x32_bf16 v[26:29], v[200:203], v[168:171], v[26:29]
	v_mfma_f32_16x16x32_bf16 v[18:21], v[192:195], v[176:179], v[18:21]
	v_mfma_f32_16x16x32_bf16 v[10:13], v[200:203], v[176:179], v[10:13]
	v_mfma_f32_16x16x32_bf16 v[6:9], v[192:195], v[184:187], v[6:9]
	v_mfma_f32_16x16x32_bf16 v[2:5], v[200:203], v[184:187], v[2:5]
	v_mfma_f32_16x16x32_bf16 v[50:53], v[196:199], v[164:167], v[50:53]
	v_mfma_f32_16x16x32_bf16 v[42:45], v[204:207], v[164:167], v[42:45]
	v_mfma_f32_16x16x32_bf16 v[34:37], v[196:199], v[172:175], v[34:37]
	v_mfma_f32_16x16x32_bf16 v[26:29], v[204:207], v[172:175], v[26:29]
	v_mfma_f32_16x16x32_bf16 v[18:21], v[196:199], v[180:183], v[18:21]
	v_mfma_f32_16x16x32_bf16 v[10:13], v[204:207], v[180:183], v[10:13]
	v_mfma_f32_16x16x32_bf16 v[6:9], v[196:199], v[188:191], v[6:9]
	v_mfma_f32_16x16x32_bf16 v[2:5], v[204:207], v[188:191], v[2:5]
	s_setprio 0
	s_add_i32 s21, s21, 2
	s_add_u32 s58, s58, 0x100
	s_addc_u32 s59, s59, 0
	s_cmp_gt_u32 s21, 29
	s_barrier
	s_cbranch_scc0 .LBB0_174
; __device__ __forceinline__ unsigned cvt_pk_bf16(float lo, float hi) { unsigned r; asm("v_cvt_pk_bf16_f32 %0, %1, %2" : "=v"(r) : "v"(lo), "v"(hi)); return r; }
;     __device__ __forceinline__ void operator()(const f32x4 (&acc)[2][2][4][2], const Unit& u, int wr, int wc, int fr, int fq) const {
;         const int row0 = u.pm * BM + wr * 64 + fr, col0 = u.pn * BM + wc * 32 + 8 * fq;
; #pragma unroll
;         for (int ai = 0; ai < 2; ++ai)
; #pragma unroll
;             for (int m = 0; m < 4; ++m) { bf16_t* rowp = O + (size_t)(row0 + ai * HALF + m * 16) * ldc + col0;
; #pragma unroll
;                 for (int bj = 0; bj < 2; ++bj) { const f32x4 v0 = acc[ai][bj][m][0], v1 = acc[ai][bj][m][1];
;                     u32x4 w; w.x = cvt_pk_bf16(v0[0], v0[1]); w.y = cvt_pk_bf16(v0[2], v0[3]); w.z = cvt_pk_bf16(v1[0], v1[1]); w.w = cvt_pk_bf16(v1[2], v1[3]);
;                     *(u32x4*)(rowp + bj * HALF) = w;
;     ...
;                     *(u32x4*)(rowp + bj * HALF + (size_t)1792 * 1024 * 1024) = w;
;     ...
;                 } }
	v_mov_b32_e32 v134, v0
	s_lshl_b32 s0, s0, 8
	s_add_i32 s0, s0, s82
	v_and_or_b32 v150, v134, 15, s0
	s_lshl_b32 s0, s6, 8
	v_lshrrev_b32_e32 v134, 1, v134
	v_and_or_b32 v134, v134, 24, s0
	v_or_b32_e32 v142, s83, v134
	v_ashrrev_i32_e32 v143, 31, v142
	v_mov_b64_e32 v[140:141], s[14:15]
	v_cvt_pk_bf16_f32 v70, v70, v71
	v_cvt_pk_bf16_f32 v71, v72, v73
	v_cvt_pk_bf16_f32 v72, v66, v67
	v_add_u32_e32 v66, 0x80, v150
	v_mad_i64_i32 v[148:149], s[6:7], v150, s25, v[140:141]
	v_lshlrev_b64 v[142:143], 1, v[142:143]
	v_cvt_pk_bf16_f32 v118, v118, v119
	v_cvt_pk_bf16_f32 v119, v120, v121
	v_cvt_pk_bf16_f32 v120, v110, v111
	v_or_b32_e32 v110, 16, v150
	v_mad_i64_i32 v[66:67], s[6:7], v66, s25, v[140:141]
	v_cvt_pk_bf16_f32 v50, v50, v51
	v_cvt_pk_bf16_f32 v51, v52, v53
	v_cvt_pk_bf16_f32 v52, v42, v43
	v_add_u32_e32 v42, 0x90, v150
	v_lshl_add_u64 v[148:149], v[148:149], 0, v[142:143]
	v_mad_i64_i32 v[110:111], s[6:7], v110, s25, v[140:141]
	v_cvt_pk_bf16_f32 v102, v102, v103
	v_cvt_pk_bf16_f32 v103, v104, v105
	v_cvt_pk_bf16_f32 v104, v94, v95
	v_or_b32_e32 v94, 32, v150
	v_lshl_add_u64 v[66:67], v[66:67], 0, v[142:143]
	v_mad_i64_i32 v[42:43], s[6:7], v42, s25, v[140:141]
	v_cvt_pk_bf16_f32 v34, v34, v35
	v_cvt_pk_bf16_f32 v35, v36, v37
	v_cvt_pk_bf16_f32 v36, v26, v27
	v_add_u32_e32 v26, 0xa0, v150
	v_cvt_pk_bf16_f32 v121, v112, v113
	global_store_dwordx4 v[148:149], v[118:121], off offset:256
	v_mad_i64_i32 v[94:95], s[6:7], v94, s25, v[140:141]
	s_nop 0
	v_lshl_add_u64 v[118:119], v[110:111], 0, v[142:143]
	v_cvt_pk_bf16_f32 v86, v86, v87
	v_cvt_pk_bf16_f32 v87, v88, v89
	v_cvt_pk_bf16_f32 v88, v78, v79
	v_or_b32_e32 v78, 48, v150
	v_cvt_pk_bf16_f32 v53, v44, v45
	global_store_dwordx4 v[66:67], v[50:53], off offset:256
	v_mad_i64_i32 v[26:27], s[6:7], v26, s25, v[140:141]
	s_nop 0
	v_lshl_add_u64 v[50:51], v[42:43], 0, v[142:143]
	v_cvt_pk_bf16_f32 v18, v18, v19
	v_cvt_pk_bf16_f32 v19, v20, v21
	v_cvt_pk_bf16_f32 v20, v10, v11
	v_add_u32_e32 v10, 0xb0, v150
	v_cvt_pk_bf16_f32 v105, v96, v97
	global_store_dwordx4 v[118:119], v[102:105], off offset:256
	v_mad_i64_i32 v[78:79], s[6:7], v78, s25, v[140:141]
	s_nop 0
	v_lshl_add_u64 v[102:103], v[94:95], 0, v[142:143]
	v_cvt_pk_bf16_f32 v37, v28, v29
	global_store_dwordx4 v[50:51], v[34:37], off offset:256
	v_mad_i64_i32 v[10:11], s[6:7], v10, s25, v[140:141]
	s_nop 0
	v_lshl_add_u64 v[34:35], v[26:27], 0, v[142:143]
	v_cvt_pk_bf16_f32 v89, v80, v81
	global_store_dwordx4 v[102:103], v[86:89], off offset:256
	v_cvt_pk_bf16_f32 v21, v12, v13
	global_store_dwordx4 v[34:35], v[18:21], off offset:256
	s_cmp_lg_u32 s1, s86
	v_lshl_add_u64 v[86:87], v[78:79], 0, v[142:143]
	v_lshl_add_u64 v[18:19], v[10:11], 0, v[142:143]
	s_mov_b32 s96, s2
	v_cvt_pk_bf16_f32 v126, v126, v127
	v_cvt_pk_bf16_f32 v127, v128, v129
	v_cvt_pk_bf16_f32 v128, v122, v123
	v_cvt_pk_bf16_f32 v129, v124, v125
	global_store_dwordx4 v[148:149], v[126:129], off
	v_cvt_pk_bf16_f32 v110, v114, v115
	v_cvt_pk_bf16_f32 v111, v116, v117
	v_cvt_pk_bf16_f32 v112, v106, v107
	v_cvt_pk_bf16_f32 v113, v108, v109
	global_store_dwordx4 v[118:119], v[110:113], off
	v_cvt_pk_bf16_f32 v94, v98, v99
	v_cvt_pk_bf16_f32 v95, v100, v101
	v_cvt_pk_bf16_f32 v96, v90, v91
	v_cvt_pk_bf16_f32 v97, v92, v93
	global_store_dwordx4 v[102:103], v[94:97], off
	v_cvt_pk_bf16_f32 v78, v82, v83
	v_cvt_pk_bf16_f32 v79, v84, v85
	v_cvt_pk_bf16_f32 v80, v74, v75
	v_cvt_pk_bf16_f32 v81, v76, v77
	global_store_dwordx4 v[86:87], v[78:81], off
	v_cvt_pk_bf16_f32 v73, v68, v69
	global_store_dwordx4 v[86:87], v[70:73], off offset:256
	v_cvt_pk_bf16_f32 v62, v62, v63
	v_cvt_pk_bf16_f32 v63, v64, v65
	v_cvt_pk_bf16_f32 v64, v58, v59
	v_cvt_pk_bf16_f32 v65, v60, v61
	global_store_dwordx4 v[66:67], v[62:65], off
	v_cvt_pk_bf16_f32 v42, v54, v55
	v_cvt_pk_bf16_f32 v43, v56, v57
	v_cvt_pk_bf16_f32 v44, v46, v47
	v_cvt_pk_bf16_f32 v45, v48, v49
	global_store_dwordx4 v[50:51], v[42:45], off
	v_cvt_pk_bf16_f32 v26, v38, v39
	v_cvt_pk_bf16_f32 v27, v40, v41
	v_cvt_pk_bf16_f32 v28, v30, v31
	v_cvt_pk_bf16_f32 v29, v32, v33
	global_store_dwordx4 v[34:35], v[26:29], off
	v_cvt_pk_bf16_f32 v10, v22, v23
	v_cvt_pk_bf16_f32 v11, v24, v25
	v_cvt_pk_bf16_f32 v12, v14, v15
	v_cvt_pk_bf16_f32 v13, v16, v17
	global_store_dwordx4 v[18:19], v[10:13], off
	v_cvt_pk_bf16_f32 v6, v6, v7
	v_cvt_pk_bf16_f32 v7, v8, v9
	v_cvt_pk_bf16_f32 v8, v2, v3
	v_cvt_pk_bf16_f32 v9, v4, v5
	global_store_dwordx4 v[18:19], v[6:9], off offset:256
	s_cbranch_scc1 .LBB0_170
	s_branch .Lbc_entry
	s_waitcnt vmcnt(0)
	s_mov_b64 s[0:1], exec
	v_readlane_b32 s6, v255, 24
	v_readlane_b32 s7, v255, 25
	s_and_b64 s[6:7], s[0:1], s[6:7]
	s_mov_b64 exec, s[6:7]
	s_cbranch_execz .LBB0_178
	s_barrier
